# combined: cvt dwordx4 stores via DPP pair exchange, Q loads nt, gemm_out tile loads sc1, 64B loop alignment
# speedup vs baseline: 1.0034x; 1.0034x over previous
.LBB0_16:
	v_add_co_u32_e32 v18, vcc, 0x1000, v4
	global_load_dwordx4 v[6:9], v[4:5], off nt
	s_nop 0
	v_addc_co_u32_e32 v19, vcc, 0, v5, vcc
	v_add_co_u32_e32 v20, vcc, 0x2000, v4
	s_nop 1
	v_addc_co_u32_e32 v21, vcc, 0, v5, vcc
	v_add_co_u32_e32 v4, vcc, 0x3000, v4
	global_load_dwordx4 v[10:13], v[18:19], off nt
	global_load_dwordx4 v[14:17], v[20:21], off nt
	v_addc_co_u32_e32 v5, vcc, 0, v5, vcc
	global_load_dwordx4 v[18:21], v[4:5], off nt
	v_and_b32_e32 v22, 1, v0
	v_cmp_eq_u32_e64 s[8:9], 1, v22
	v_mov_b32_e32 v23, 0x7f8
	s_waitcnt lgkmcnt(0)
	v_lshl_add_u64 v[2:3], v[2:3], 1, s[4:5]
	v_cndmask_b32_e64 v22, 0, v23, s[8:9]
	v_add_co_u32_e32 v2, vcc, v2, v22
	s_nop 1
	v_addc_co_u32_e32 v3, vcc, 0, v3, vcc
	v_add_co_u32_e32 v4, vcc, 0x1000, v2
	s_nop 1
	v_addc_co_u32_e32 v5, vcc, 0, v3, vcc
	s_waitcnt vmcnt(2)
	v_cvt_pk_f16_f32 v6, v6, v7
	v_cvt_pk_f16_f32 v7, v8, v9
	v_cvt_pk_f16_f32 v8, v10, v11
	v_cvt_pk_f16_f32 v9, v12, v13
	v_cndmask_b32_e64 v10, v8, v6, s[8:9]
	v_cndmask_b32_e64 v11, v9, v7, s[8:9]
	s_nop 1
	v_mov_b32_dpp v12, v10 quad_perm:[1,0,3,2] row_mask:0xf bank_mask:0xf
	v_mov_b32_dpp v13, v11 quad_perm:[1,0,3,2] row_mask:0xf bank_mask:0xf
	v_cndmask_b32_e64 v22, v6, v12, s[8:9]
	v_cndmask_b32_e64 v23, v7, v13, s[8:9]
	v_cndmask_b32_e64 v24, v12, v8, s[8:9]
	v_cndmask_b32_e64 v25, v13, v9, s[8:9]
	global_store_dwordx4 v[2:3], v[22:25], off sc1
	s_waitcnt vmcnt(1)
	v_cvt_pk_f16_f32 v6, v14, v15
	v_cvt_pk_f16_f32 v7, v16, v17
	v_cvt_pk_f16_f32 v8, v18, v19
	v_cvt_pk_f16_f32 v9, v20, v21
	v_cndmask_b32_e64 v10, v8, v6, s[8:9]
	v_cndmask_b32_e64 v11, v9, v7, s[8:9]
	s_nop 1
	v_mov_b32_dpp v12, v10 quad_perm:[1,0,3,2] row_mask:0xf bank_mask:0xf
	v_mov_b32_dpp v13, v11 quad_perm:[1,0,3,2] row_mask:0xf bank_mask:0xf
	v_cndmask_b32_e64 v14, v6, v12, s[8:9]
	v_cndmask_b32_e64 v15, v7, v13, s[8:9]
	v_cndmask_b32_e64 v16, v12, v8, s[8:9]
	v_cndmask_b32_e64 v17, v13, v9, s[8:9]
	global_store_dwordx4 v[4:5], v[14:17], off sc1
	s_cmp_gt_u32 s2, 11
	s_cbranch_scc1 .LBB0_26
	s_load_dwordx2 s[4:5], s[0:1], 0x48
	v_lshl_or_b32 v0, s2, 8, v0
	s_movk_i32 s2, 0x3ff
	v_cmp_lt_u32_e32 vcc, s2, v0
	v_mov_b32_e32 v1, 0
	s_and_saveexec_b64 s[2:3], vcc
	s_xor_b64 s[2:3], exec, s[2:3]
	s_cbranch_execz .LBB0_23
	s_movk_i32 s6, 0x7ff
	v_cmp_lt_u32_e32 vcc, s6, v0
	s_and_saveexec_b64 s[6:7], vcc
	s_xor_b64 s[6:7], exec, s[6:7]
	s_cbranch_execz .LBB0_20
	s_load_dwordx2 s[8:9], s[0:1], 0x40
	s_waitcnt lgkmcnt(0)
	v_lshl_add_u64 v[2:3], v[0:1], 2, s[8:9]
	s_movk_i32 s8, 0xe000
	s_mov_b32 s9, -1
	v_lshl_add_u64 v[2:3], v[2:3], 0, s[8:9]

	.amdhsa_kernel _Z7cvt_allPKfS0_S0_S0_S0_PDF16_S0_S0_S0_Pf
		.amdhsa_group_segment_fixed_size 0
		.amdhsa_private_segment_fixed_size 0
		.amdhsa_kernarg_size 80
		.amdhsa_user_sgpr_count 2
		.amdhsa_user_sgpr_dispatch_ptr 0
		.amdhsa_user_sgpr_queue_ptr 0
		.amdhsa_user_sgpr_kernarg_segment_ptr 1
		.amdhsa_user_sgpr_dispatch_id 0
		.amdhsa_user_sgpr_kernarg_preload_length 0
		.amdhsa_user_sgpr_kernarg_preload_offset 0
		.amdhsa_user_sgpr_private_segment_size 0
		.amdhsa_uses_dynamic_stack 0
		.amdhsa_enable_private_segment 0
		.amdhsa_system_sgpr_workgroup_id_x 1
		.amdhsa_system_sgpr_workgroup_id_y 0
		.amdhsa_system_sgpr_workgroup_id_z 0
		.amdhsa_system_sgpr_workgroup_info 0
		.amdhsa_system_vgpr_workitem_id 0
		.amdhsa_next_free_vgpr 26
		.amdhsa_next_free_sgpr 10
		.amdhsa_accum_offset 28
		.amdhsa_reserve_vcc 1
		.amdhsa_float_round_mode_32 0
		.amdhsa_float_round_mode_16_64 0
		.amdhsa_float_denorm_mode_32 3
		.amdhsa_float_denorm_mode_16_64 3
		.amdhsa_dx10_clamp 1
		.amdhsa_ieee_mode 1
		.amdhsa_fp16_overflow 0
		.amdhsa_tg_split 0
		.amdhsa_exception_fp_ieee_invalid_op 0
		.amdhsa_exception_fp_denorm_src 0
		.amdhsa_exception_fp_ieee_div_zero 0
		.amdhsa_exception_fp_ieee_overflow 0
		.amdhsa_exception_fp_ieee_underflow 0
		.amdhsa_exception_fp_ieee_inexact 0
		.amdhsa_exception_int_div_zero 0
	.end_amdhsa_kernel

_ZN6g128w88gemm_outEPKDF16_S1_PKfPf:
	s_load_dword s12, s[0:1], 0x20
	s_and_b32 s14, s2, 7
	s_load_dwordx8 s[4:11], s[0:1], 0x0
	s_ashr_i32 s1, s2, 3
	v_lshlrev_b32_e32 v1, 4, v0
	s_waitcnt lgkmcnt(0)
	s_lshr_b32 s0, s12, 3
	s_mul_i32 s0, s0, s14
	s_add_i32 s1, s0, s1
	s_ashr_i32 s0, s1, 31
	s_lshr_b32 s0, s0, 29
	s_add_i32 s2, s1, s0
	s_lshl_b32 s0, s2, 4
	s_movk_i32 s12, 0x70
	s_and_b32 s2, s2, 0x1fffff8
	v_bitop3_b32 v1, v1, s12, v0 bitop3:0x48
	v_lshlrev_b32_e32 v2, 8, v0
	s_mov_b32 s12, 0x1f800
	s_sub_i32 s1, s1, s2
	v_readfirstlane_b32 s3, v0
	s_and_b32 s0, s0, 0xffffff80
	v_and_or_b32 v10, v2, s12, v1
	v_or_b32_e32 v2, 0x20000, v2
	s_mov_b32 s12, 0x3f800
	s_lshl_b32 s2, s1, 7
	s_lshr_b32 s13, s3, 6
	s_bfe_u32 s19, s3, 0x20006
	v_and_or_b32 v20, v2, s12, v1
	s_lshr_b32 s12, s3, 8
	s_ashr_i32 s1, s0, 31
	s_ashr_i32 s3, s2, 31
	s_lshl_b64 s[14:15], s[0:1], 11
	s_lshl_b64 s[16:17], s[2:3], 11
	s_add_u32 s16, s6, s16
	s_addc_u32 s17, s7, s17
	s_add_u32 s14, s4, s14
	s_addc_u32 s15, s5, s15
	s_lshl_b64 s[2:3], s[2:3], 2
	s_add_u32 s4, s8, s2
	s_addc_u32 s5, s9, s3
	s_lshl_b32 s1, s19, 7
	v_bfe_u32 v22, v0, 4, 2
	s_add_u32 s4, s4, s1
	s_addc_u32 s5, s5, 0
	v_lshlrev_b32_e32 v1, 4, v22
	s_lshl_b32 s13, s13, 10
	global_load_dwordx4 v[6:9], v1, s[4:5]
	global_load_dwordx4 v[2:5], v1, s[4:5] offset:64
	s_add_i32 s5, s13, 0
	s_add_i32 s4, s5, 0x4000
	s_mov_b32 m0, s5
	s_add_i32 s6, s5, 0x2000
	global_load_lds_dwordx4 v10, s[14:15] sc1
	s_mov_b32 m0, s4
	v_mov_b32_e32 v11, 0
	global_load_lds_dwordx4 v10, s[16:17] sc1
	s_mov_b32 m0, s6
	s_add_i32 s7, s5, 0x6000
	v_mov_b32_e32 v21, v11
	global_load_lds_dwordx4 v20, s[14:15] sc1
	s_mov_b32 m0, s7
	v_lshl_add_u64 v[12:13], s[14:15], 0, v[10:11]
	v_lshl_add_u64 v[14:15], s[16:17], 0, v[10:11]
	v_lshl_add_u64 v[18:19], s[16:17], 0, v[20:21]
	global_load_lds_dwordx4 v20, s[16:17] sc1
	s_add_i32 s17, s5, 0x8000
	s_mov_b64 s[8:9], 0x80
	v_lshl_add_u64 v[16:17], s[14:15], 0, v[20:21]
	s_add_i32 s15, s5, 0xc000
	v_lshl_add_u64 v[20:21], v[12:13], 0, s[8:9]
	s_mov_b32 m0, s17
	s_add_i32 s16, s5, 0xa000
	global_load_lds_dwordx4 v[20:21], off sc1
	v_lshl_add_u64 v[20:21], v[14:15], 0, s[8:9]
	s_mov_b32 m0, s15
	s_add_i32 s18, s5, 0xe000
	global_load_lds_dwordx4 v[20:21], off sc1
	v_lshl_add_u64 v[20:21], v[16:17], 0, s[8:9]
	s_mov_b32 m0, s16
	s_add_i32 s22, 0, 0x10000
	global_load_lds_dwordx4 v[20:21], off sc1
	v_lshl_add_u64 v[20:21], v[18:19], 0, s[8:9]
	s_mov_b32 m0, s18
	s_add_i32 s13, s22, s13
	global_load_lds_dwordx4 v[20:21], off sc1
	s_waitcnt vmcnt(4)
	s_mov_b64 s[20:21], 0x100
	s_waitcnt lgkmcnt(0)
	s_barrier
	s_add_i32 s8, s5, 0x14000
	v_lshl_add_u64 v[20:21], v[12:13], 0, s[20:21]
	s_mov_b32 m0, s13
	s_add_i32 s9, s13, 0x2000
	global_load_lds_dwordx4 v[20:21], off sc1
	v_lshl_add_u64 v[20:21], v[14:15], 0, s[20:21]
	s_mov_b32 m0, s8
	s_add_i32 s14, s5, 0x16000
	global_load_lds_dwordx4 v[20:21], off sc1
	v_lshl_add_u64 v[20:21], v[16:17], 0, s[20:21]
	s_mov_b32 m0, s9
	v_and_b32_e32 v10, 15, v0
	global_load_lds_dwordx4 v[20:21], off sc1
	v_lshl_add_u64 v[20:21], v[18:19], 0, s[20:21]
	s_mov_b32 m0, s14
	v_bfe_u32 v24, v0, 1, 3
	global_load_lds_dwordx4 v[20:21], off sc1
	v_lshrrev_b32_e32 v20, 4, v0
	v_lshlrev_b32_e32 v21, 7, v10
	v_bitop3_b32 v20, v20, v24, 3 bitop3:0x6c
	v_lshl_or_b32 v23, s12, 13, v21
	v_lshl_or_b32 v72, s19, 12, v21
	v_lshlrev_b32_e32 v73, 4, v20
	v_bitop3_b32 v20, v22, v24, 4 bitop3:0x36
	v_or_b32_e32 v108, v73, v23
	v_lshlrev_b32_e32 v74, 4, v20
	v_or_b32_e32 v20, v73, v72
	v_or_b32_e32 v109, v74, v23
	v_add_u32_e32 v20, 0, v20
	v_or_b32_e32 v21, v74, v72
	v_add_u32_e32 v22, 0, v108
	v_add_u32_e32 v21, 0, v21
	ds_read_b128 v[24:27], v20 offset:16384
	ds_read_b128 v[28:31], v20 offset:18432
	ds_read_b128 v[32:35], v21 offset:16384
	ds_read_b128 v[36:39], v21 offset:18432
	v_add_u32_e32 v23, 0, v109
	ds_read_b128 v[40:43], v22
	ds_read_b128 v[44:47], v22 offset:2048
	ds_read_b128 v[48:51], v23
	ds_read_b128 v[52:55], v23 offset:2048
	ds_read_b128 v[56:59], v22 offset:4096
	ds_read_b128 v[60:63], v22 offset:6144
	ds_read_b128 v[64:67], v23 offset:4096
	ds_read_b128 v[68:71], v23 offset:6144
	v_or_b32_e32 v72, 0x4000, v72
	v_or_b32_e32 v104, v73, v72
	v_or_b32_e32 v105, v74, v72
	s_setprio 1
	s_waitcnt lgkmcnt(0)
	v_mfma_f32_16x16x32_f16 v[72:75], v[24:27], v[40:43], 0
	v_mfma_f32_16x16x32_f16 v[40:43], v[28:31], v[40:43], 0
	v_mfma_f32_16x16x32_f16 v[76:79], v[24:27], v[44:47], 0
	v_mfma_f32_16x16x32_f16 v[44:47], v[28:31], v[44:47], 0
	v_mfma_f32_16x16x32_f16 v[80:83], v[24:27], v[56:59], 0
	v_mfma_f32_16x16x32_f16 v[56:59], v[28:31], v[56:59], 0
	v_mfma_f32_16x16x32_f16 v[24:27], v[24:27], v[60:63], 0
	v_mfma_f32_16x16x32_f16 v[28:31], v[28:31], v[60:63], 0
	v_mfma_f32_16x16x32_f16 v[60:63], v[32:35], v[48:51], v[72:75]
	v_mfma_f32_16x16x32_f16 v[40:43], v[36:39], v[48:51], v[40:43]
	v_mfma_f32_16x16x32_f16 v[48:51], v[32:35], v[52:55], v[76:79]
	v_mfma_f32_16x16x32_f16 v[44:47], v[36:39], v[52:55], v[44:47]
	v_mfma_f32_16x16x32_f16 v[52:55], v[32:35], v[64:67], v[80:83]
	v_mfma_f32_16x16x32_f16 v[56:59], v[36:39], v[64:67], v[56:59]
	v_mfma_f32_16x16x32_f16 v[24:27], v[32:35], v[68:71], v[24:27]
	v_mfma_f32_16x16x32_f16 v[28:31], v[36:39], v[68:71], v[28:31]
	s_setprio 0
	s_waitcnt vmcnt(4)
	s_mov_b64 s[20:21], 0x180
	s_mov_b32 m0, s5
	s_waitcnt lgkmcnt(0)
	s_barrier
	v_lshl_add_u64 v[32:33], v[12:13], 0, s[20:21]
	global_load_lds_dwordx4 v[32:33], off sc1
	v_lshl_add_u64 v[32:33], v[14:15], 0, s[20:21]
	s_mov_b32 m0, s4
	s_nop 0
	global_load_lds_dwordx4 v[32:33], off sc1
	v_lshl_add_u64 v[32:33], v[16:17], 0, s[20:21]
	s_mov_b32 m0, s6
	s_nop 0
	global_load_lds_dwordx4 v[32:33], off sc1
	v_lshl_add_u64 v[32:33], v[18:19], 0, s[20:21]
	s_mov_b32 m0, s7
	s_nop 0
	global_load_lds_dwordx4 v[32:33], off sc1
	ds_read_b128 v[32:35], v20 offset:49152
	ds_read_b128 v[36:39], v20 offset:51200
	ds_read_b128 v[64:67], v21 offset:49152
	ds_read_b128 v[68:71], v21 offset:51200
	ds_read_b128 v[72:75], v22 offset:32768
	ds_read_b128 v[76:79], v22 offset:34816
	ds_read_b128 v[80:83], v23 offset:32768
	ds_read_b128 v[84:87], v23 offset:34816
	ds_read_b128 v[88:91], v22 offset:36864
	ds_read_b128 v[92:95], v22 offset:38912
	ds_read_b128 v[96:99], v23 offset:36864
	ds_read_b128 v[100:103], v23 offset:38912
	s_setprio 1
	s_waitcnt lgkmcnt(0)
	v_mfma_f32_16x16x32_f16 v[60:63], v[32:35], v[72:75], v[60:63]
	v_mfma_f32_16x16x32_f16 v[40:43], v[36:39], v[72:75], v[40:43]
	v_mfma_f32_16x16x32_f16 v[48:51], v[32:35], v[76:79], v[48:51]
	v_mfma_f32_16x16x32_f16 v[44:47], v[36:39], v[76:79], v[44:47]
	v_mfma_f32_16x16x32_f16 v[52:55], v[32:35], v[88:91], v[52:55]
	v_mfma_f32_16x16x32_f16 v[56:59], v[36:39], v[88:91], v[56:59]
	v_mfma_f32_16x16x32_f16 v[24:27], v[32:35], v[92:95], v[24:27]
	v_mfma_f32_16x16x32_f16 v[28:31], v[36:39], v[92:95], v[28:31]
	v_mfma_f32_16x16x32_f16 v[36:39], v[64:67], v[80:83], v[60:63]
	v_mfma_f32_16x16x32_f16 v[40:43], v[68:71], v[80:83], v[40:43]
	v_mfma_f32_16x16x32_f16 v[48:51], v[64:67], v[84:87], v[48:51]
	v_mfma_f32_16x16x32_f16 v[44:47], v[68:71], v[84:87], v[44:47]
	v_mfma_f32_16x16x32_f16 v[52:55], v[64:67], v[96:99], v[52:55]
	v_mfma_f32_16x16x32_f16 v[56:59], v[68:71], v[96:99], v[56:59]
	v_mfma_f32_16x16x32_f16 v[60:63], v[64:67], v[100:103], v[24:27]
	v_mfma_f32_16x16x32_f16 v[64:67], v[68:71], v[100:103], v[28:31]
	s_setprio 0
	s_waitcnt vmcnt(4)
	s_mov_b64 s[20:21], 0x200
	s_mov_b32 m0, s17
	s_waitcnt lgkmcnt(0)
	s_barrier
	v_lshl_add_u64 v[24:25], v[12:13], 0, s[20:21]
	global_load_lds_dwordx4 v[24:25], off sc1
	v_lshl_add_u64 v[24:25], v[14:15], 0, s[20:21]
	s_mov_b32 m0, s15
	s_add_i32 s19, 0, 0x10800
	global_load_lds_dwordx4 v[24:25], off sc1
	v_lshl_add_u64 v[24:25], v[16:17], 0, s[20:21]
	s_mov_b32 m0, s16
	v_add_u32_e32 v26, s19, v104
	global_load_lds_dwordx4 v[24:25], off sc1
	v_lshl_add_u64 v[24:25], v[18:19], 0, s[20:21]
	s_mov_b32 m0, s18
	v_add_u32_e32 v27, s19, v105
	global_load_lds_dwordx4 v[24:25], off sc1
	v_add_u32_e32 v30, s19, v108
	v_add_u32_e32 v31, s19, v109
	s_add_i32 s19, 0, 0x11000
	v_add_u32_e32 v32, s19, v108
	v_add_u32_e32 v33, s19, v109
	s_add_i32 s19, 0, 0x11800
	v_add_u32_e32 v24, s22, v104
	v_add_u32_e32 v28, s22, v108
	v_add_u32_e32 v34, s19, v108
	v_add_u32_e32 v25, s22, v105
	ds_read_b128 v[68:71], v24
	ds_read_b128 v[72:75], v25
	ds_read_b128 v[76:79], v26
	ds_read_b128 v[80:83], v27
	v_add_u32_e32 v29, s22, v109
	ds_read_b128 v[84:87], v28
	ds_read_b128 v[88:91], v29
	ds_read_b128 v[92:95], v30
	ds_read_b128 v[96:99], v31
	ds_read_b128 v[100:103], v32
	ds_read_b128 v[104:107], v33
	v_add_u32_e32 v35, s19, v109
	ds_read_b128 v[108:111], v34
	ds_read_b128 v[112:115], v35
	s_setprio 1
	s_waitcnt lgkmcnt(0)
	v_mfma_f32_16x16x32_f16 v[36:39], v[68:71], v[84:87], v[36:39]
	v_mfma_f32_16x16x32_f16 v[40:43], v[76:79], v[84:87], v[40:43]
	v_mfma_f32_16x16x32_f16 v[48:51], v[68:71], v[92:95], v[48:51]
	v_mfma_f32_16x16x32_f16 v[44:47], v[76:79], v[92:95], v[44:47]
	v_mfma_f32_16x16x32_f16 v[52:55], v[68:71], v[100:103], v[52:55]
	v_mfma_f32_16x16x32_f16 v[56:59], v[76:79], v[100:103], v[56:59]
	v_mfma_f32_16x16x32_f16 v[60:63], v[68:71], v[108:111], v[60:63]
	v_mfma_f32_16x16x32_f16 v[64:67], v[76:79], v[108:111], v[64:67]
	v_mfma_f32_16x16x32_f16 v[36:39], v[72:75], v[88:91], v[36:39]
	v_mfma_f32_16x16x32_f16 v[40:43], v[80:83], v[88:91], v[40:43]
	v_mfma_f32_16x16x32_f16 v[48:51], v[72:75], v[96:99], v[48:51]
	v_mfma_f32_16x16x32_f16 v[44:47], v[80:83], v[96:99], v[44:47]
	v_mfma_f32_16x16x32_f16 v[52:55], v[72:75], v[104:107], v[52:55]
	v_mfma_f32_16x16x32_f16 v[56:59], v[80:83], v[104:107], v[56:59]
	v_mfma_f32_16x16x32_f16 v[60:63], v[72:75], v[112:115], v[60:63]
	v_mfma_f32_16x16x32_f16 v[64:67], v[80:83], v[112:115], v[64:67]
	s_setprio 0
	s_waitcnt vmcnt(4)
	s_mov_b64 s[20:21], 0x280
	s_mov_b32 m0, s13
	s_waitcnt lgkmcnt(0)
	s_barrier
	v_lshl_add_u64 v[68:69], v[12:13], 0, s[20:21]
	global_load_lds_dwordx4 v[68:69], off sc1
	v_lshl_add_u64 v[68:69], v[14:15], 0, s[20:21]
	s_mov_b32 m0, s8
	s_nop 0
	global_load_lds_dwordx4 v[68:69], off sc1
	v_lshl_add_u64 v[68:69], v[16:17], 0, s[20:21]
	s_mov_b32 m0, s9
	s_nop 0
	global_load_lds_dwordx4 v[68:69], off sc1
	v_lshl_add_u64 v[68:69], v[18:19], 0, s[20:21]
	s_mov_b32 m0, s14
	s_nop 0
	global_load_lds_dwordx4 v[68:69], off sc1
	ds_read_b128 v[68:71], v20 offset:16384
	ds_read_b128 v[72:75], v20 offset:18432
	ds_read_b128 v[76:79], v21 offset:16384
	ds_read_b128 v[80:83], v21 offset:18432
	ds_read_b128 v[84:87], v22
	ds_read_b128 v[88:91], v22 offset:2048
	ds_read_b128 v[92:95], v23
	ds_read_b128 v[96:99], v23 offset:2048
	ds_read_b128 v[100:103], v22 offset:4096
	ds_read_b128 v[104:107], v22 offset:6144
	ds_read_b128 v[108:111], v23 offset:4096
	ds_read_b128 v[112:115], v23 offset:6144
	s_setprio 1
	s_waitcnt lgkmcnt(0)
	v_mfma_f32_16x16x32_f16 v[36:39], v[68:71], v[84:87], v[36:39]
	v_mfma_f32_16x16x32_f16 v[40:43], v[72:75], v[84:87], v[40:43]
	v_mfma_f32_16x16x32_f16 v[48:51], v[68:71], v[88:91], v[48:51]
	v_mfma_f32_16x16x32_f16 v[44:47], v[72:75], v[88:91], v[44:47]
	v_mfma_f32_16x16x32_f16 v[52:55], v[68:71], v[100:103], v[52:55]
	v_mfma_f32_16x16x32_f16 v[56:59], v[72:75], v[100:103], v[56:59]
	v_mfma_f32_16x16x32_f16 v[60:63], v[68:71], v[104:107], v[60:63]
	v_mfma_f32_16x16x32_f16 v[64:67], v[72:75], v[104:107], v[64:67]
	v_mfma_f32_16x16x32_f16 v[36:39], v[76:79], v[92:95], v[36:39]
	v_mfma_f32_16x16x32_f16 v[40:43], v[80:83], v[92:95], v[40:43]
	v_mfma_f32_16x16x32_f16 v[48:51], v[76:79], v[96:99], v[48:51]
	v_mfma_f32_16x16x32_f16 v[44:47], v[80:83], v[96:99], v[44:47]
	v_mfma_f32_16x16x32_f16 v[52:55], v[76:79], v[108:111], v[52:55]
	v_mfma_f32_16x16x32_f16 v[56:59], v[80:83], v[108:111], v[56:59]
	v_mfma_f32_16x16x32_f16 v[60:63], v[76:79], v[112:115], v[60:63]
	v_mfma_f32_16x16x32_f16 v[64:67], v[80:83], v[112:115], v[64:67]
	s_setprio 0
	s_waitcnt vmcnt(4)
	s_mov_b64 s[20:21], 0x300
	s_mov_b32 m0, s5
	s_waitcnt lgkmcnt(0)
	s_barrier
	v_lshl_add_u64 v[68:69], v[12:13], 0, s[20:21]
	global_load_lds_dwordx4 v[68:69], off sc1
	v_lshl_add_u64 v[68:69], v[14:15], 0, s[20:21]
	s_mov_b32 m0, s4
	s_nop 0
	global_load_lds_dwordx4 v[68:69], off sc1
	v_lshl_add_u64 v[68:69], v[16:17], 0, s[20:21]
	s_mov_b32 m0, s6
	s_nop 0
	global_load_lds_dwordx4 v[68:69], off sc1
	v_lshl_add_u64 v[68:69], v[18:19], 0, s[20:21]
	s_mov_b32 m0, s7
	s_nop 0
	global_load_lds_dwordx4 v[68:69], off sc1
	ds_read_b128 v[68:71], v20 offset:49152
	ds_read_b128 v[72:75], v20 offset:51200
	ds_read_b128 v[76:79], v21 offset:49152
	ds_read_b128 v[80:83], v21 offset:51200
	ds_read_b128 v[84:87], v22 offset:32768
	ds_read_b128 v[88:91], v22 offset:34816
	ds_read_b128 v[92:95], v23 offset:32768
	ds_read_b128 v[96:99], v23 offset:34816
	ds_read_b128 v[100:103], v22 offset:36864
	ds_read_b128 v[104:107], v22 offset:38912
	ds_read_b128 v[108:111], v23 offset:36864
	ds_read_b128 v[112:115], v23 offset:38912
	s_setprio 1
	s_waitcnt lgkmcnt(0)
	v_mfma_f32_16x16x32_f16 v[36:39], v[68:71], v[84:87], v[36:39]
	v_mfma_f32_16x16x32_f16 v[40:43], v[72:75], v[84:87], v[40:43]
	v_mfma_f32_16x16x32_f16 v[48:51], v[68:71], v[88:91], v[48:51]
	v_mfma_f32_16x16x32_f16 v[44:47], v[72:75], v[88:91], v[44:47]
	v_mfma_f32_16x16x32_f16 v[52:55], v[68:71], v[100:103], v[52:55]
	v_mfma_f32_16x16x32_f16 v[56:59], v[72:75], v[100:103], v[56:59]
	v_mfma_f32_16x16x32_f16 v[60:63], v[68:71], v[104:107], v[60:63]
	v_mfma_f32_16x16x32_f16 v[64:67], v[72:75], v[104:107], v[64:67]
	v_mfma_f32_16x16x32_f16 v[36:39], v[76:79], v[92:95], v[36:39]
	v_mfma_f32_16x16x32_f16 v[40:43], v[80:83], v[92:95], v[40:43]
	v_mfma_f32_16x16x32_f16 v[48:51], v[76:79], v[96:99], v[48:51]
	v_mfma_f32_16x16x32_f16 v[44:47], v[80:83], v[96:99], v[44:47]
	v_mfma_f32_16x16x32_f16 v[52:55], v[76:79], v[108:111], v[52:55]
	v_mfma_f32_16x16x32_f16 v[56:59], v[80:83], v[108:111], v[56:59]
	v_mfma_f32_16x16x32_f16 v[60:63], v[76:79], v[112:115], v[60:63]
	v_mfma_f32_16x16x32_f16 v[64:67], v[80:83], v[112:115], v[64:67]
	s_setprio 0
	s_waitcnt vmcnt(4)
	s_mov_b64 s[20:21], 0x380
	s_mov_b32 m0, s17
	s_waitcnt lgkmcnt(0)
	s_barrier
	v_lshl_add_u64 v[68:69], v[12:13], 0, s[20:21]
	global_load_lds_dwordx4 v[68:69], off sc1
	v_lshl_add_u64 v[68:69], v[14:15], 0, s[20:21]
	s_mov_b32 m0, s15
	s_nop 0
	global_load_lds_dwordx4 v[68:69], off sc1
	v_lshl_add_u64 v[68:69], v[16:17], 0, s[20:21]
	s_mov_b32 m0, s16
	s_nop 0
	global_load_lds_dwordx4 v[68:69], off sc1
	v_lshl_add_u64 v[68:69], v[18:19], 0, s[20:21]
	s_mov_b32 m0, s18
	s_nop 0
	global_load_lds_dwordx4 v[68:69], off sc1
	ds_read_b128 v[68:71], v24
	ds_read_b128 v[72:75], v25
	ds_read_b128 v[76:79], v26
	ds_read_b128 v[80:83], v27
	ds_read_b128 v[84:87], v28
	ds_read_b128 v[88:91], v29
	ds_read_b128 v[92:95], v30
	ds_read_b128 v[96:99], v31
	ds_read_b128 v[100:103], v32
	ds_read_b128 v[104:107], v33
	ds_read_b128 v[108:111], v34
	ds_read_b128 v[112:115], v35
	s_setprio 1
	s_waitcnt lgkmcnt(0)
	v_mfma_f32_16x16x32_f16 v[36:39], v[68:71], v[84:87], v[36:39]
	v_mfma_f32_16x16x32_f16 v[40:43], v[76:79], v[84:87], v[40:43]
	v_mfma_f32_16x16x32_f16 v[48:51], v[68:71], v[92:95], v[48:51]
	v_mfma_f32_16x16x32_f16 v[44:47], v[76:79], v[92:95], v[44:47]
	v_mfma_f32_16x16x32_f16 v[52:55], v[68:71], v[100:103], v[52:55]
	v_mfma_f32_16x16x32_f16 v[56:59], v[76:79], v[100:103], v[56:59]
	v_mfma_f32_16x16x32_f16 v[60:63], v[68:71], v[108:111], v[60:63]
	v_mfma_f32_16x16x32_f16 v[64:67], v[76:79], v[108:111], v[64:67]
	v_mfma_f32_16x16x32_f16 v[36:39], v[72:75], v[88:91], v[36:39]
	v_mfma_f32_16x16x32_f16 v[40:43], v[80:83], v[88:91], v[40:43]
	v_mfma_f32_16x16x32_f16 v[48:51], v[72:75], v[96:99], v[48:51]
	v_mfma_f32_16x16x32_f16 v[44:47], v[80:83], v[96:99], v[44:47]
	v_mfma_f32_16x16x32_f16 v[52:55], v[72:75], v[104:107], v[52:55]
	v_mfma_f32_16x16x32_f16 v[56:59], v[80:83], v[104:107], v[56:59]
	v_mfma_f32_16x16x32_f16 v[60:63], v[72:75], v[112:115], v[60:63]
	v_mfma_f32_16x16x32_f16 v[64:67], v[80:83], v[112:115], v[64:67]
	s_setprio 0
	s_waitcnt vmcnt(4)
	s_mov_b64 s[20:21], 0x400
	s_mov_b32 m0, s13
	s_waitcnt lgkmcnt(0)
	s_barrier
	v_lshl_add_u64 v[68:69], v[12:13], 0, s[20:21]
	global_load_lds_dwordx4 v[68:69], off sc1
	v_lshl_add_u64 v[68:69], v[14:15], 0, s[20:21]
	s_mov_b32 m0, s8
	s_nop 0
	global_load_lds_dwordx4 v[68:69], off sc1
	v_lshl_add_u64 v[68:69], v[16:17], 0, s[20:21]
	s_mov_b32 m0, s9
	s_nop 0
	global_load_lds_dwordx4 v[68:69], off sc1
	v_lshl_add_u64 v[68:69], v[18:19], 0, s[20:21]
	s_mov_b32 m0, s14
	s_nop 0
	global_load_lds_dwordx4 v[68:69], off sc1
	ds_read_b128 v[68:71], v20 offset:16384
	ds_read_b128 v[72:75], v20 offset:18432
	ds_read_b128 v[76:79], v21 offset:16384
	ds_read_b128 v[80:83], v21 offset:18432
	ds_read_b128 v[84:87], v22
	ds_read_b128 v[88:91], v22 offset:2048
	ds_read_b128 v[92:95], v23
	ds_read_b128 v[96:99], v23 offset:2048
	ds_read_b128 v[100:103], v22 offset:4096
	ds_read_b128 v[104:107], v22 offset:6144
	ds_read_b128 v[108:111], v23 offset:4096
	ds_read_b128 v[112:115], v23 offset:6144
	s_setprio 1
	s_waitcnt lgkmcnt(0)
	v_mfma_f32_16x16x32_f16 v[36:39], v[68:71], v[84:87], v[36:39]
	v_mfma_f32_16x16x32_f16 v[40:43], v[72:75], v[84:87], v[40:43]
	v_mfma_f32_16x16x32_f16 v[48:51], v[68:71], v[88:91], v[48:51]
	v_mfma_f32_16x16x32_f16 v[44:47], v[72:75], v[88:91], v[44:47]
	v_mfma_f32_16x16x32_f16 v[52:55], v[68:71], v[100:103], v[52:55]
	v_mfma_f32_16x16x32_f16 v[56:59], v[72:75], v[100:103], v[56:59]
	v_mfma_f32_16x16x32_f16 v[60:63], v[68:71], v[104:107], v[60:63]
	v_mfma_f32_16x16x32_f16 v[64:67], v[72:75], v[104:107], v[64:67]
	v_mfma_f32_16x16x32_f16 v[36:39], v[76:79], v[92:95], v[36:39]
	v_mfma_f32_16x16x32_f16 v[40:43], v[80:83], v[92:95], v[40:43]
	v_mfma_f32_16x16x32_f16 v[48:51], v[76:79], v[96:99], v[48:51]
	v_mfma_f32_16x16x32_f16 v[44:47], v[80:83], v[96:99], v[44:47]
	v_mfma_f32_16x16x32_f16 v[52:55], v[76:79], v[108:111], v[52:55]
	v_mfma_f32_16x16x32_f16 v[56:59], v[80:83], v[108:111], v[56:59]
	v_mfma_f32_16x16x32_f16 v[60:63], v[76:79], v[112:115], v[60:63]
	v_mfma_f32_16x16x32_f16 v[64:67], v[80:83], v[112:115], v[64:67]
	s_setprio 0
	s_waitcnt vmcnt(4)
	s_mov_b64 s[20:21], 0x480
	s_mov_b32 m0, s5
	s_waitcnt lgkmcnt(0)
	s_barrier
	v_lshl_add_u64 v[68:69], v[12:13], 0, s[20:21]
	global_load_lds_dwordx4 v[68:69], off sc1
	v_lshl_add_u64 v[68:69], v[14:15], 0, s[20:21]
	s_mov_b32 m0, s4
	s_nop 0
	global_load_lds_dwordx4 v[68:69], off sc1
	v_lshl_add_u64 v[68:69], v[16:17], 0, s[20:21]
	s_mov_b32 m0, s6
	s_nop 0
	global_load_lds_dwordx4 v[68:69], off sc1
	v_lshl_add_u64 v[68:69], v[18:19], 0, s[20:21]
	s_mov_b32 m0, s7
	s_nop 0
	global_load_lds_dwordx4 v[68:69], off sc1
	ds_read_b128 v[68:71], v20 offset:49152
	ds_read_b128 v[72:75], v20 offset:51200
	ds_read_b128 v[76:79], v21 offset:49152
	ds_read_b128 v[80:83], v21 offset:51200
	ds_read_b128 v[84:87], v22 offset:32768
	ds_read_b128 v[88:91], v22 offset:34816
	ds_read_b128 v[92:95], v23 offset:32768
	ds_read_b128 v[96:99], v23 offset:34816
	ds_read_b128 v[100:103], v22 offset:36864
	ds_read_b128 v[104:107], v22 offset:38912
	ds_read_b128 v[108:111], v23 offset:36864
	ds_read_b128 v[112:115], v23 offset:38912
	s_setprio 1
	s_waitcnt lgkmcnt(0)
	v_mfma_f32_16x16x32_f16 v[36:39], v[68:71], v[84:87], v[36:39]
	v_mfma_f32_16x16x32_f16 v[40:43], v[72:75], v[84:87], v[40:43]
	v_mfma_f32_16x16x32_f16 v[48:51], v[68:71], v[88:91], v[48:51]
	v_mfma_f32_16x16x32_f16 v[44:47], v[72:75], v[88:91], v[44:47]
	v_mfma_f32_16x16x32_f16 v[52:55], v[68:71], v[100:103], v[52:55]
	v_mfma_f32_16x16x32_f16 v[56:59], v[72:75], v[100:103], v[56:59]
	v_mfma_f32_16x16x32_f16 v[60:63], v[68:71], v[104:107], v[60:63]
	v_mfma_f32_16x16x32_f16 v[64:67], v[72:75], v[104:107], v[64:67]
	v_mfma_f32_16x16x32_f16 v[36:39], v[76:79], v[92:95], v[36:39]
	v_mfma_f32_16x16x32_f16 v[40:43], v[80:83], v[92:95], v[40:43]
	v_mfma_f32_16x16x32_f16 v[48:51], v[76:79], v[96:99], v[48:51]
	v_mfma_f32_16x16x32_f16 v[44:47], v[80:83], v[96:99], v[44:47]
	v_mfma_f32_16x16x32_f16 v[52:55], v[76:79], v[108:111], v[52:55]
	v_mfma_f32_16x16x32_f16 v[56:59], v[80:83], v[108:111], v[56:59]
	v_mfma_f32_16x16x32_f16 v[60:63], v[76:79], v[112:115], v[60:63]
	v_mfma_f32_16x16x32_f16 v[64:67], v[80:83], v[112:115], v[64:67]
	s_setprio 0
	s_waitcnt vmcnt(4)
	s_mov_b64 s[20:21], 0x500
	s_mov_b32 m0, s17
	s_waitcnt lgkmcnt(0)
	s_barrier
	v_lshl_add_u64 v[68:69], v[12:13], 0, s[20:21]
	global_load_lds_dwordx4 v[68:69], off sc1
	v_lshl_add_u64 v[68:69], v[14:15], 0, s[20:21]
	s_mov_b32 m0, s15
	s_nop 0
	global_load_lds_dwordx4 v[68:69], off sc1
	v_lshl_add_u64 v[68:69], v[16:17], 0, s[20:21]
	s_mov_b32 m0, s16
	s_nop 0
	global_load_lds_dwordx4 v[68:69], off sc1
	v_lshl_add_u64 v[68:69], v[18:19], 0, s[20:21]
	s_mov_b32 m0, s18
	s_nop 0
	global_load_lds_dwordx4 v[68:69], off sc1
	ds_read_b128 v[68:71], v24
	ds_read_b128 v[72:75], v25
	ds_read_b128 v[76:79], v26
	ds_read_b128 v[80:83], v27
	ds_read_b128 v[84:87], v28
	ds_read_b128 v[88:91], v29
	ds_read_b128 v[92:95], v30
	ds_read_b128 v[96:99], v31
	ds_read_b128 v[100:103], v32
	ds_read_b128 v[104:107], v33
	ds_read_b128 v[108:111], v34
	ds_read_b128 v[112:115], v35
	s_setprio 1
	s_waitcnt lgkmcnt(0)
	v_mfma_f32_16x16x32_f16 v[36:39], v[68:71], v[84:87], v[36:39]
	v_mfma_f32_16x16x32_f16 v[40:43], v[76:79], v[84:87], v[40:43]
	v_mfma_f32_16x16x32_f16 v[48:51], v[68:71], v[92:95], v[48:51]
	v_mfma_f32_16x16x32_f16 v[44:47], v[76:79], v[92:95], v[44:47]
	v_mfma_f32_16x16x32_f16 v[52:55], v[68:71], v[100:103], v[52:55]
	v_mfma_f32_16x16x32_f16 v[56:59], v[76:79], v[100:103], v[56:59]
	v_mfma_f32_16x16x32_f16 v[60:63], v[68:71], v[108:111], v[60:63]
	v_mfma_f32_16x16x32_f16 v[64:67], v[76:79], v[108:111], v[64:67]
	v_mfma_f32_16x16x32_f16 v[36:39], v[72:75], v[88:91], v[36:39]
	v_mfma_f32_16x16x32_f16 v[40:43], v[80:83], v[88:91], v[40:43]
	v_mfma_f32_16x16x32_f16 v[48:51], v[72:75], v[96:99], v[48:51]
	v_mfma_f32_16x16x32_f16 v[44:47], v[80:83], v[96:99], v[44:47]
	v_mfma_f32_16x16x32_f16 v[52:55], v[72:75], v[104:107], v[52:55]
	v_mfma_f32_16x16x32_f16 v[56:59], v[80:83], v[104:107], v[56:59]
	v_mfma_f32_16x16x32_f16 v[60:63], v[72:75], v[112:115], v[60:63]
	v_mfma_f32_16x16x32_f16 v[64:67], v[80:83], v[112:115], v[64:67]
	s_setprio 0
	s_waitcnt vmcnt(4)
	s_mov_b64 s[20:21], 0x580
	s_mov_b32 m0, s13
	s_waitcnt lgkmcnt(0)
	s_barrier
	v_lshl_add_u64 v[68:69], v[12:13], 0, s[20:21]
	global_load_lds_dwordx4 v[68:69], off sc1
	v_lshl_add_u64 v[68:69], v[14:15], 0, s[20:21]
	s_mov_b32 m0, s8
	s_nop 0
	global_load_lds_dwordx4 v[68:69], off sc1
	v_lshl_add_u64 v[68:69], v[16:17], 0, s[20:21]
	s_mov_b32 m0, s9
	s_nop 0
	global_load_lds_dwordx4 v[68:69], off sc1
	v_lshl_add_u64 v[68:69], v[18:19], 0, s[20:21]
	s_mov_b32 m0, s14
	s_nop 0
	global_load_lds_dwordx4 v[68:69], off sc1
	ds_read_b128 v[68:71], v20 offset:16384
	ds_read_b128 v[72:75], v20 offset:18432
	ds_read_b128 v[76:79], v21 offset:16384
	ds_read_b128 v[80:83], v21 offset:18432
	ds_read_b128 v[84:87], v22
	ds_read_b128 v[88:91], v22 offset:2048
	ds_read_b128 v[92:95], v23
	ds_read_b128 v[96:99], v23 offset:2048
	ds_read_b128 v[100:103], v22 offset:4096
	ds_read_b128 v[104:107], v22 offset:6144
	ds_read_b128 v[108:111], v23 offset:4096
	ds_read_b128 v[112:115], v23 offset:6144
	s_setprio 1
	s_waitcnt lgkmcnt(0)
	v_mfma_f32_16x16x32_f16 v[36:39], v[68:71], v[84:87], v[36:39]
	v_mfma_f32_16x16x32_f16 v[40:43], v[72:75], v[84:87], v[40:43]
	v_mfma_f32_16x16x32_f16 v[48:51], v[68:71], v[88:91], v[48:51]
	v_mfma_f32_16x16x32_f16 v[44:47], v[72:75], v[88:91], v[44:47]
	v_mfma_f32_16x16x32_f16 v[52:55], v[68:71], v[100:103], v[52:55]
	v_mfma_f32_16x16x32_f16 v[56:59], v[72:75], v[100:103], v[56:59]
	v_mfma_f32_16x16x32_f16 v[60:63], v[68:71], v[104:107], v[60:63]
	v_mfma_f32_16x16x32_f16 v[64:67], v[72:75], v[104:107], v[64:67]
	v_mfma_f32_16x16x32_f16 v[36:39], v[76:79], v[92:95], v[36:39]
	v_mfma_f32_16x16x32_f16 v[40:43], v[80:83], v[92:95], v[40:43]
	v_mfma_f32_16x16x32_f16 v[48:51], v[76:79], v[96:99], v[48:51]
	v_mfma_f32_16x16x32_f16 v[44:47], v[80:83], v[96:99], v[44:47]
	v_mfma_f32_16x16x32_f16 v[52:55], v[76:79], v[108:111], v[52:55]
	v_mfma_f32_16x16x32_f16 v[56:59], v[80:83], v[108:111], v[56:59]
	v_mfma_f32_16x16x32_f16 v[60:63], v[76:79], v[112:115], v[60:63]
	v_mfma_f32_16x16x32_f16 v[64:67], v[80:83], v[112:115], v[64:67]
	s_setprio 0
	s_waitcnt vmcnt(4)
	s_mov_b64 s[20:21], 0x600
	s_mov_b32 m0, s5
	s_waitcnt lgkmcnt(0)
	s_barrier
	v_lshl_add_u64 v[68:69], v[12:13], 0, s[20:21]
	global_load_lds_dwordx4 v[68:69], off sc1
	v_lshl_add_u64 v[68:69], v[14:15], 0, s[20:21]
	s_mov_b32 m0, s4
	s_nop 0
	global_load_lds_dwordx4 v[68:69], off sc1
	v_lshl_add_u64 v[68:69], v[16:17], 0, s[20:21]
	s_mov_b32 m0, s6
	s_nop 0
	global_load_lds_dwordx4 v[68:69], off sc1
	v_lshl_add_u64 v[68:69], v[18:19], 0, s[20:21]
	s_mov_b32 m0, s7
	s_nop 0
	global_load_lds_dwordx4 v[68:69], off sc1
	ds_read_b128 v[68:71], v20 offset:49152
	ds_read_b128 v[72:75], v20 offset:51200
	ds_read_b128 v[76:79], v21 offset:49152
	ds_read_b128 v[80:83], v21 offset:51200
	ds_read_b128 v[84:87], v22 offset:32768
	ds_read_b128 v[88:91], v22 offset:34816
	ds_read_b128 v[92:95], v23 offset:32768
	ds_read_b128 v[96:99], v23 offset:34816
	ds_read_b128 v[100:103], v22 offset:36864
	ds_read_b128 v[104:107], v22 offset:38912
	ds_read_b128 v[108:111], v23 offset:36864
	ds_read_b128 v[112:115], v23 offset:38912
	s_setprio 1
	s_waitcnt lgkmcnt(0)
	v_mfma_f32_16x16x32_f16 v[36:39], v[68:71], v[84:87], v[36:39]
	v_mfma_f32_16x16x32_f16 v[40:43], v[72:75], v[84:87], v[40:43]
	v_mfma_f32_16x16x32_f16 v[48:51], v[68:71], v[88:91], v[48:51]
	v_mfma_f32_16x16x32_f16 v[44:47], v[72:75], v[88:91], v[44:47]
	v_mfma_f32_16x16x32_f16 v[52:55], v[68:71], v[100:103], v[52:55]
	v_mfma_f32_16x16x32_f16 v[56:59], v[72:75], v[100:103], v[56:59]
	v_mfma_f32_16x16x32_f16 v[60:63], v[68:71], v[104:107], v[60:63]
	v_mfma_f32_16x16x32_f16 v[64:67], v[72:75], v[104:107], v[64:67]
	v_mfma_f32_16x16x32_f16 v[36:39], v[76:79], v[92:95], v[36:39]
	v_mfma_f32_16x16x32_f16 v[40:43], v[80:83], v[92:95], v[40:43]
	v_mfma_f32_16x16x32_f16 v[48:51], v[76:79], v[96:99], v[48:51]
	v_mfma_f32_16x16x32_f16 v[44:47], v[80:83], v[96:99], v[44:47]
	v_mfma_f32_16x16x32_f16 v[52:55], v[76:79], v[108:111], v[52:55]
	v_mfma_f32_16x16x32_f16 v[56:59], v[80:83], v[108:111], v[56:59]
	v_mfma_f32_16x16x32_f16 v[60:63], v[76:79], v[112:115], v[60:63]
	v_mfma_f32_16x16x32_f16 v[64:67], v[80:83], v[112:115], v[64:67]
	s_setprio 0
	s_waitcnt vmcnt(4)
	s_mov_b64 s[20:21], 0x680
	s_mov_b32 m0, s17
	s_waitcnt lgkmcnt(0)
	s_barrier
	v_lshl_add_u64 v[68:69], v[12:13], 0, s[20:21]
	global_load_lds_dwordx4 v[68:69], off sc1
	v_lshl_add_u64 v[68:69], v[14:15], 0, s[20:21]
	s_mov_b32 m0, s15
	s_nop 0
	global_load_lds_dwordx4 v[68:69], off sc1
	v_lshl_add_u64 v[68:69], v[16:17], 0, s[20:21]
	s_mov_b32 m0, s16
	s_nop 0
	global_load_lds_dwordx4 v[68:69], off sc1
	v_lshl_add_u64 v[68:69], v[18:19], 0, s[20:21]
	s_mov_b32 m0, s18
	s_nop 0
	global_load_lds_dwordx4 v[68:69], off sc1
	ds_read_b128 v[68:71], v24
	ds_read_b128 v[72:75], v25
	ds_read_b128 v[76:79], v26
	ds_read_b128 v[80:83], v27
	ds_read_b128 v[84:87], v28
	ds_read_b128 v[88:91], v29
	ds_read_b128 v[92:95], v30
	ds_read_b128 v[96:99], v31
	ds_read_b128 v[100:103], v32
	ds_read_b128 v[104:107], v33
	ds_read_b128 v[108:111], v34
	ds_read_b128 v[112:115], v35
	s_setprio 1
	s_waitcnt lgkmcnt(0)
	v_mfma_f32_16x16x32_f16 v[36:39], v[68:71], v[84:87], v[36:39]
	v_mfma_f32_16x16x32_f16 v[40:43], v[76:79], v[84:87], v[40:43]
	v_mfma_f32_16x16x32_f16 v[48:51], v[68:71], v[92:95], v[48:51]
	v_mfma_f32_16x16x32_f16 v[44:47], v[76:79], v[92:95], v[44:47]
	v_mfma_f32_16x16x32_f16 v[52:55], v[68:71], v[100:103], v[52:55]
	v_mfma_f32_16x16x32_f16 v[56:59], v[76:79], v[100:103], v[56:59]
	v_mfma_f32_16x16x32_f16 v[60:63], v[68:71], v[108:111], v[60:63]
	v_mfma_f32_16x16x32_f16 v[64:67], v[76:79], v[108:111], v[64:67]
	v_mfma_f32_16x16x32_f16 v[36:39], v[72:75], v[88:91], v[36:39]
	v_mfma_f32_16x16x32_f16 v[40:43], v[80:83], v[88:91], v[40:43]
	v_mfma_f32_16x16x32_f16 v[48:51], v[72:75], v[96:99], v[48:51]
	v_mfma_f32_16x16x32_f16 v[44:47], v[80:83], v[96:99], v[44:47]
	v_mfma_f32_16x16x32_f16 v[52:55], v[72:75], v[104:107], v[52:55]
	v_mfma_f32_16x16x32_f16 v[56:59], v[80:83], v[104:107], v[56:59]
	v_mfma_f32_16x16x32_f16 v[60:63], v[72:75], v[112:115], v[60:63]
	v_mfma_f32_16x16x32_f16 v[64:67], v[80:83], v[112:115], v[64:67]
	s_setprio 0
	s_waitcnt vmcnt(4)
	s_mov_b64 s[16:17], 0x700
	s_mov_b32 m0, s13
	s_waitcnt lgkmcnt(0)
	s_barrier
	v_lshl_add_u64 v[68:69], v[12:13], 0, s[16:17]
	global_load_lds_dwordx4 v[68:69], off sc1
	v_lshl_add_u64 v[68:69], v[14:15], 0, s[16:17]
	s_mov_b32 m0, s8
	s_nop 0
	global_load_lds_dwordx4 v[68:69], off sc1
	v_lshl_add_u64 v[68:69], v[16:17], 0, s[16:17]
	s_mov_b32 m0, s9
	s_nop 0
	global_load_lds_dwordx4 v[68:69], off sc1
	v_lshl_add_u64 v[68:69], v[18:19], 0, s[16:17]
	s_mov_b32 m0, s14
	s_nop 0
	global_load_lds_dwordx4 v[68:69], off sc1
	ds_read_b128 v[68:71], v20 offset:16384
	ds_read_b128 v[72:75], v20 offset:18432
	ds_read_b128 v[76:79], v21 offset:16384
	ds_read_b128 v[80:83], v21 offset:18432
	ds_read_b128 v[84:87], v22
	ds_read_b128 v[88:91], v22 offset:2048
	ds_read_b128 v[92:95], v23
	ds_read_b128 v[96:99], v23 offset:2048
	ds_read_b128 v[100:103], v22 offset:4096
	ds_read_b128 v[104:107], v22 offset:6144
	ds_read_b128 v[108:111], v23 offset:4096
	ds_read_b128 v[112:115], v23 offset:6144
	s_setprio 1
	s_waitcnt lgkmcnt(0)
	v_mfma_f32_16x16x32_f16 v[36:39], v[68:71], v[84:87], v[36:39]
	v_mfma_f32_16x16x32_f16 v[40:43], v[72:75], v[84:87], v[40:43]
	v_mfma_f32_16x16x32_f16 v[48:51], v[68:71], v[88:91], v[48:51]
	v_mfma_f32_16x16x32_f16 v[44:47], v[72:75], v[88:91], v[44:47]
	v_mfma_f32_16x16x32_f16 v[52:55], v[68:71], v[100:103], v[52:55]
	v_mfma_f32_16x16x32_f16 v[56:59], v[72:75], v[100:103], v[56:59]
	v_mfma_f32_16x16x32_f16 v[60:63], v[68:71], v[104:107], v[60:63]
	v_mfma_f32_16x16x32_f16 v[64:67], v[72:75], v[104:107], v[64:67]
	v_mfma_f32_16x16x32_f16 v[36:39], v[76:79], v[92:95], v[36:39]
	v_mfma_f32_16x16x32_f16 v[40:43], v[80:83], v[92:95], v[40:43]
	v_mfma_f32_16x16x32_f16 v[48:51], v[76:79], v[96:99], v[48:51]
	v_mfma_f32_16x16x32_f16 v[44:47], v[80:83], v[96:99], v[44:47]
	v_mfma_f32_16x16x32_f16 v[52:55], v[76:79], v[108:111], v[52:55]
	v_mfma_f32_16x16x32_f16 v[56:59], v[80:83], v[108:111], v[56:59]
	v_mfma_f32_16x16x32_f16 v[60:63], v[76:79], v[112:115], v[60:63]
	v_mfma_f32_16x16x32_f16 v[64:67], v[80:83], v[112:115], v[64:67]
	s_setprio 0
	s_waitcnt vmcnt(4)
	s_mov_b64 s[8:9], 0x780
	s_mov_b32 m0, s5
	s_waitcnt lgkmcnt(0)
	s_barrier
	v_lshl_add_u64 v[12:13], v[12:13], 0, s[8:9]
	global_load_lds_dwordx4 v[12:13], off sc1
	v_lshl_add_u64 v[12:13], v[14:15], 0, s[8:9]
	s_mov_b32 m0, s4
	s_nop 0
	global_load_lds_dwordx4 v[12:13], off sc1
	v_lshl_add_u64 v[12:13], v[16:17], 0, s[8:9]
	s_mov_b32 m0, s6
	s_nop 0
	global_load_lds_dwordx4 v[12:13], off sc1
	v_lshl_add_u64 v[12:13], v[18:19], 0, s[8:9]
	s_mov_b32 m0, s7
	s_nop 0
	global_load_lds_dwordx4 v[12:13], off sc1
	ds_read_b128 v[12:15], v20 offset:49152
	ds_read_b128 v[16:19], v20 offset:51200
	ds_read_b128 v[68:71], v21 offset:49152
	ds_read_b128 v[72:75], v21 offset:51200
	ds_read_b128 v[76:79], v22 offset:32768
	ds_read_b128 v[80:83], v22 offset:34816
	ds_read_b128 v[84:87], v23 offset:32768
	ds_read_b128 v[88:91], v23 offset:34816
	ds_read_b128 v[92:95], v22 offset:36864
	ds_read_b128 v[96:99], v22 offset:38912
	ds_read_b128 v[100:103], v23 offset:36864
	ds_read_b128 v[104:107], v23 offset:38912
	s_setprio 1
	s_waitcnt lgkmcnt(0)
	v_mfma_f32_16x16x32_f16 v[36:39], v[12:15], v[76:79], v[36:39]
	v_mfma_f32_16x16x32_f16 v[40:43], v[16:19], v[76:79], v[40:43]
	v_mfma_f32_16x16x32_f16 v[48:51], v[12:15], v[80:83], v[48:51]
	v_mfma_f32_16x16x32_f16 v[44:47], v[16:19], v[80:83], v[44:47]
	v_mfma_f32_16x16x32_f16 v[52:55], v[12:15], v[92:95], v[52:55]
	v_mfma_f32_16x16x32_f16 v[56:59], v[16:19], v[92:95], v[56:59]
	v_mfma_f32_16x16x32_f16 v[12:15], v[12:15], v[96:99], v[60:63]
	v_mfma_f32_16x16x32_f16 v[16:19], v[16:19], v[96:99], v[64:67]
	v_mfma_f32_16x16x32_f16 v[36:39], v[68:71], v[84:87], v[36:39]
	v_mfma_f32_16x16x32_f16 v[40:43], v[72:75], v[84:87], v[40:43]
	v_mfma_f32_16x16x32_f16 v[48:51], v[68:71], v[88:91], v[48:51]
	v_mfma_f32_16x16x32_f16 v[44:47], v[72:75], v[88:91], v[44:47]
	v_mfma_f32_16x16x32_f16 v[52:55], v[68:71], v[100:103], v[52:55]
	v_mfma_f32_16x16x32_f16 v[56:59], v[72:75], v[100:103], v[56:59]
	v_mfma_f32_16x16x32_f16 v[12:15], v[68:71], v[104:107], v[12:15]
	v_mfma_f32_16x16x32_f16 v[16:19], v[72:75], v[104:107], v[16:19]
	s_setprio 0
	s_waitcnt vmcnt(4)
	s_waitcnt lgkmcnt(0)
	s_barrier
	ds_read_b128 v[60:63], v35
	ds_read_b128 v[64:67], v34
	ds_read_b128 v[68:71], v33
	ds_read_b128 v[32:35], v32
	ds_read_b128 v[72:75], v31
	ds_read_b128 v[76:79], v30
	ds_read_b128 v[80:83], v29
	ds_read_b128 v[28:31], v28
	ds_read_b128 v[84:87], v27
	ds_read_b128 v[88:91], v26
	ds_read_b128 v[92:95], v25
	ds_read_b128 v[24:27], v24
	s_setprio 1
	s_waitcnt lgkmcnt(0)
	v_mfma_f32_16x16x32_f16 v[36:39], v[24:27], v[28:31], v[36:39]
	v_mfma_f32_16x16x32_f16 v[28:31], v[88:91], v[28:31], v[40:43]
	v_mfma_f32_16x16x32_f16 v[40:43], v[24:27], v[76:79], v[48:51]
	v_mfma_f32_16x16x32_f16 v[44:47], v[88:91], v[76:79], v[44:47]
	v_mfma_f32_16x16x32_f16 v[48:51], v[24:27], v[32:35], v[52:55]
	v_mfma_f32_16x16x32_f16 v[32:35], v[88:91], v[32:35], v[56:59]
	v_mfma_f32_16x16x32_f16 v[12:15], v[24:27], v[64:67], v[12:15]
	v_mfma_f32_16x16x32_f16 v[16:19], v[88:91], v[64:67], v[16:19]
	v_mfma_f32_16x16x32_f16 v[24:27], v[92:95], v[80:83], v[36:39]
	v_mfma_f32_16x16x32_f16 v[28:31], v[84:87], v[80:83], v[28:31]
	v_mfma_f32_16x16x32_f16 v[36:39], v[92:95], v[72:75], v[40:43]
	v_mfma_f32_16x16x32_f16 v[40:43], v[84:87], v[72:75], v[44:47]
	v_mfma_f32_16x16x32_f16 v[44:47], v[92:95], v[68:71], v[48:51]
	v_mfma_f32_16x16x32_f16 v[32:35], v[84:87], v[68:71], v[32:35]
	v_mfma_f32_16x16x32_f16 v[12:15], v[92:95], v[60:63], v[12:15]
	v_mfma_f32_16x16x32_f16 v[16:19], v[84:87], v[60:63], v[16:19]
	s_setprio 0
	s_waitcnt vmcnt(0)
	s_waitcnt lgkmcnt(0)
	s_barrier
	ds_read_b128 v[48:51], v23 offset:6144
	ds_read_b128 v[52:55], v23 offset:4096
	ds_read_b128 v[56:59], v22 offset:6144
	ds_read_b128 v[60:63], v22 offset:4096
	ds_read_b128 v[64:67], v23 offset:2048
	ds_read_b128 v[68:71], v23
	ds_read_b128 v[72:75], v22 offset:2048
	ds_read_b128 v[76:79], v22
	ds_read_b128 v[80:83], v21 offset:18432
	ds_read_b128 v[84:87], v21 offset:16384
	ds_read_b128 v[88:91], v20 offset:18432
	ds_read_b128 v[20:23], v20 offset:16384
	s_setprio 1
	s_waitcnt lgkmcnt(0)
	v_mfma_f32_16x16x32_f16 v[24:27], v[20:23], v[76:79], v[24:27]
	v_mfma_f32_16x16x32_f16 v[28:31], v[88:91], v[76:79], v[28:31]
	v_mfma_f32_16x16x32_f16 v[36:39], v[20:23], v[72:75], v[36:39]
	v_mfma_f32_16x16x32_f16 v[40:43], v[88:91], v[72:75], v[40:43]
	v_mfma_f32_16x16x32_f16 v[44:47], v[20:23], v[60:63], v[44:47]
	v_mfma_f32_16x16x32_f16 v[32:35], v[88:91], v[60:63], v[32:35]
	v_mfma_f32_16x16x32_f16 v[12:15], v[20:23], v[56:59], v[12:15]
	v_mfma_f32_16x16x32_f16 v[16:19], v[88:91], v[56:59], v[16:19]
	v_mfma_f32_16x16x32_f16 v[20:23], v[84:87], v[68:71], v[24:27]
	v_mfma_f32_16x16x32_f16 v[24:27], v[80:83], v[68:71], v[28:31]
	v_mfma_f32_16x16x32_f16 v[28:31], v[84:87], v[64:67], v[36:39]
	v_mfma_f32_16x16x32_f16 v[36:39], v[80:83], v[64:67], v[40:43]
	v_mfma_f32_16x16x32_f16 v[40:43], v[84:87], v[52:55], v[44:47]
	v_mfma_f32_16x16x32_f16 v[32:35], v[80:83], v[52:55], v[32:35]
	v_mfma_f32_16x16x32_f16 v[12:15], v[84:87], v[48:51], v[12:15]
	v_mfma_f32_16x16x32_f16 v[16:19], v[80:83], v[48:51], v[16:19]
	s_setprio 0
	v_lshl_or_b32 v10, s12, 6, v10
	s_movk_i32 s4, 0x210
	s_add_i32 s1, s1, 0
	v_mul_lo_u32 v10, v10, s4
	s_waitcnt vmcnt(0)
	v_pk_add_f32 v[22:23], v[8:9], v[22:23]
	v_pk_add_f32 v[20:21], v[6:7], v[20:21]
	v_add3_u32 v1, s1, v1, v10
	s_waitcnt lgkmcnt(0)
	s_barrier
	ds_write_b128 v1, v[20:23]
	v_pk_add_f32 v[22:23], v[8:9], v[30:31]
	v_pk_add_f32 v[20:21], v[6:7], v[28:29]
	ds_write_b128 v1, v[20:23] offset:8448
	v_pk_add_f32 v[22:23], v[8:9], v[42:43]
	v_pk_add_f32 v[20:21], v[6:7], v[40:41]
	v_pk_add_f32 v[8:9], v[8:9], v[14:15]
	v_pk_add_f32 v[6:7], v[6:7], v[12:13]
	ds_write_b128 v1, v[6:9] offset:25344
	v_pk_add_f32 v[8:9], v[4:5], v[26:27]
	v_pk_add_f32 v[6:7], v[2:3], v[24:25]
	ds_write_b128 v1, v[6:9] offset:64
	v_pk_add_f32 v[8:9], v[4:5], v[38:39]
	v_pk_add_f32 v[6:7], v[2:3], v[36:37]
	ds_write_b128 v1, v[6:9] offset:8512
	v_pk_add_f32 v[8:9], v[4:5], v[34:35]
	v_pk_add_f32 v[6:7], v[2:3], v[32:33]
	v_pk_add_f32 v[4:5], v[4:5], v[18:19]
	v_pk_add_f32 v[2:3], v[2:3], v[16:17]
	ds_write_b128 v1, v[20:23] offset:16896
	ds_write_b128 v1, v[6:9] offset:16960
	ds_write_b128 v1, v[2:5] offset:25408
	v_and_b32_e32 v1, 31, v0
	v_lshlrev_b32_e32 v10, 4, v1
	v_add_u32_e32 v1, 0, v10
	v_lshrrev_b32_e32 v6, 5, v0
	s_waitcnt lgkmcnt(0)
	s_barrier
	v_mad_u32_u24 v20, v6, s4, v1
	ds_read_b128 v[2:5], v20
	s_add_u32 s2, s10, s2
	v_or_b32_e32 v16, s0, v6
	s_addc_u32 s3, s11, s3
	v_ashrrev_i32_e32 v17, 31, v16
	v_lshl_add_u64 v[14:15], s[2:3], 0, v[10:11]
	v_lshlrev_b64 v[6:7], 12, v[16:17]
	v_lshl_add_u64 v[10:11], v[14:15], 0, v[6:7]
	ds_read_b128 v[6:9], v20 offset:16896
	s_waitcnt lgkmcnt(1)
	global_store_dwordx4 v[10:11], v[2:5], off sc1
	s_nop 1
	v_or_b32_e32 v2, 0x200, v0
	v_lshrrev_b32_e32 v10, 5, v2
	v_mad_u32_u24 v2, v10, s4, v1
	v_or_b32_e32 v10, s0, v10
	ds_read_b128 v[2:5], v2
	v_ashrrev_i32_e32 v11, 31, v10
	v_lshlrev_b64 v[10:11], 12, v[10:11]
	v_lshl_add_u64 v[18:19], v[14:15], 0, v[10:11]
	v_or_b32_e32 v10, 0x600, v0
	v_lshrrev_b32_e32 v17, 5, v10
	v_mad_u32_u24 v10, v17, s4, v1
	ds_read_b128 v[10:13], v10
	s_waitcnt lgkmcnt(1)
	global_store_dwordx4 v[18:19], v[2:5], off sc1
	s_nop 1
	v_or_b32_e32 v2, 32, v16
	v_ashrrev_i32_e32 v3, 31, v2
	v_lshlrev_b64 v[2:3], 12, v[2:3]
	v_lshl_add_u64 v[2:3], v[14:15], 0, v[2:3]
	global_store_dwordx4 v[2:3], v[6:9], off sc1
	v_or_b32_e32 v2, s0, v17
	v_ashrrev_i32_e32 v3, 31, v2
	v_lshlrev_b64 v[2:3], 12, v[2:3]
	v_lshl_add_u64 v[2:3], v[14:15], 0, v[2:3]
	s_waitcnt lgkmcnt(0)
	global_store_dwordx4 v[2:3], v[10:13], off sc1
	ds_read_b128 v[2:5], v20 offset:33792
	v_or_b32_e32 v6, 64, v16
	v_ashrrev_i32_e32 v7, 31, v6
	v_lshlrev_b64 v[6:7], 12, v[6:7]
	v_lshl_add_u64 v[10:11], v[14:15], 0, v[6:7]
	ds_read_b128 v[6:9], v20 offset:50688
	s_waitcnt lgkmcnt(1)
	global_store_dwordx4 v[10:11], v[2:5], off sc1
	s_nop 1
	v_or_b32_e32 v2, 0xa00, v0
	v_lshrrev_b32_e32 v10, 5, v2
	v_mad_u32_u24 v2, v10, s4, v1
	v_or_b32_e32 v10, s0, v10
	v_or_b32_e32 v0, 0xe00, v0
	v_ashrrev_i32_e32 v11, 31, v10
	v_lshrrev_b32_e32 v17, 5, v0
	ds_read_b128 v[2:5], v2
	v_lshlrev_b64 v[10:11], 12, v[10:11]
	v_mad_u32_u24 v0, v17, s4, v1
	v_lshl_add_u64 v[18:19], v[14:15], 0, v[10:11]
	ds_read_b128 v[10:13], v0
	v_or_b32_e32 v0, 0x60, v16
	v_ashrrev_i32_e32 v1, 31, v0
	v_lshlrev_b64 v[0:1], 12, v[0:1]
	v_lshl_add_u64 v[0:1], v[14:15], 0, v[0:1]
	s_waitcnt lgkmcnt(1)
	global_store_dwordx4 v[18:19], v[2:5], off sc1
	global_store_dwordx4 v[0:1], v[6:9], off sc1
	v_or_b32_e32 v0, s0, v17
	v_ashrrev_i32_e32 v1, 31, v0
	v_lshlrev_b64 v[0:1], 12, v[0:1]
	v_lshl_add_u64 v[0:1], v[14:15], 0, v[0:1]
	s_waitcnt lgkmcnt(0)
	global_store_dwordx4 v[0:1], v[10:13], off sc1
	s_endpgm

_ZN3att8attn_fwdEPKDF16_PDF16_:
	s_load_dwordx4 s[4:7], s[0:1], 0x0
	s_lshl_b32 s0, s2, 2
	s_and_b32 s0, s0, 28
	s_lshr_b32 s1, s2, 6
	v_readfirstlane_b32 s10, v0
	s_add_i32 s8, s0, s1
	s_lshl_b32 s0, s2, 5
	s_mov_b32 s9, 0
	s_lshr_b32 s26, s10, 6
	s_and_b32 s27, s0, 0x700
	s_lshl_b64 s[0:1], s[8:9], 11
	s_or_b32 s0, s0, s27
	s_lshl_b32 s28, s26, 5
	s_add_u32 s0, s0, s28
	s_addc_u32 s1, s1, 0
	s_lshl_b64 s[0:1], s[0:1], 7
	s_waitcnt lgkmcnt(0)
	s_add_u32 s12, s4, s0
	s_addc_u32 s13, s5, s1
	s_lshl_b64 s[2:3], s[8:9], 18
	s_add_u32 s1, s4, s2
	s_addc_u32 s15, s5, s3
	s_and_b32 s0, s10, 0x3fffffc0
	s_lshl_b32 s10, s26, 9
	s_mov_b32 s11, s9
	s_lshl_b64 s[10:11], s[10:11], 1
	v_and_b32_e32 v190, 63, v0
	s_add_u32 s14, s1, s10
	s_addc_u32 s15, s15, s11
	v_lshlrev_b32_e32 v184, 4, v190
	v_mov_b32_e32 v185, 0
	v_lshl_add_u64 v[48:49], s[14:15], 0, v[184:185]
	s_mov_b64 s[14:15], 0x800000
	s_lshl_b32 s1, s26, 10
	v_lshl_add_u64 v[180:181], v[48:49], 0, s[14:15]
	s_mov_b64 s[14:15], 0x1000000
	s_cmp_lg_u32 0, -1
	v_lshl_add_u64 v[182:183], v[48:49], 0, s[14:15]
	s_cselect_b32 s14, 0, 0
	v_bfe_u32 v192, v0, 5, 1
	s_add_i32 s30, s1, s14
	s_mov_b32 s1, m0
	s_mov_b32 m0, s30
	s_nop 0
	global_load_lds_dwordx4 v[180:181], off
	s_mov_b32 m0, s1
	v_and_b32_e32 v191, 31, v0
	s_add_i32 s31, s30, 0x6000
	s_mov_b32 s1, m0
	s_mov_b32 m0, s31
	s_nop 0
	global_load_lds_dwordx4 v[182:183], off
	s_mov_b32 m0, s1
	s_mov_b64 s[14:15], 0x802000
	v_lshlrev_b32_e32 v195, 4, v192
	v_lshl_add_u64 v[2:3], v[48:49], 0, s[14:15]
	s_add_i32 s1, s30, 0x2000
	s_mov_b32 s14, m0
	s_mov_b32 m0, s1
	s_nop 0
	global_load_lds_dwordx4 v[2:3], off
	s_mov_b32 m0, s14
	v_lshl_or_b32 v1, v191, 7, v195
	global_load_dwordx4 v[136:139], v1, s[12:13] nt
	global_load_dwordx4 v[128:131], v1, s[12:13] offset:32 nt
	global_load_dwordx4 v[120:123], v1, s[12:13] offset:64 nt
	global_load_dwordx4 v[116:119], v1, s[12:13] offset:96 nt
	s_mov_b64 s[14:15], 0x804000
	v_mov_b32_e32 v2, v185
	v_mov_b32_e32 v3, v185
	v_mov_b32_e32 v4, v185
	v_mov_b32_e32 v5, v185
	v_mov_b32_e32 v6, v185
	v_mov_b32_e32 v7, v185
	v_mov_b32_e32 v8, v185
	v_mov_b32_e32 v9, v185
	v_mov_b32_e32 v10, v185
	v_mov_b32_e32 v11, v185
	v_mov_b32_e32 v12, v185
	v_mov_b32_e32 v13, v185
	v_mov_b32_e32 v14, v185
	v_mov_b32_e32 v15, v185
	v_mov_b32_e32 v16, v185
	v_mov_b32_e32 v17, v185
	v_lshlrev_b32_e32 v1, 10, v192
	v_lshlrev_b32_e32 v18, 4, v191
	v_add3_u32 v198, 0, v1, v18
	v_lshl_add_u64 v[18:19], v[48:49], 0, s[14:15]
	s_add_i32 s1, s30, 0x4000
	s_mov_b32 s12, m0
	s_mov_b32 m0, s1
	s_nop 0
	global_load_lds_dwordx4 v[18:19], off
	s_mov_b32 m0, s12
	s_waitcnt vmcnt(3) lgkmcnt(0)
	s_barrier
	ds_read_b128 v[34:37], v198
	ds_read_b128 v[38:41], v198 offset:512
	v_lshlrev_b32_e32 v193, 3, v0
	s_mov_b64 s[16:17], 0x1002000
	s_add_i32 s1, s30, 0x8000
	s_lshl_b32 s0, s0, 2
	s_add_i32 s29, s0, 0
	s_add_u32 s2, s10, s2
	s_addc_u32 s3, s11, s3
	s_mov_b32 s20, -1
	s_movk_i32 s23, 0x2000
	s_movk_i32 s21, 0x4000
	s_mov_b64 s[10:11], 0x2000
	s_mov_b32 s22, 0x41000000
	s_mov_b64 s[14:15], 0x4000
	v_lshl_add_u32 v196, v191, 2, s29
	v_mov_b32_e32 v199, 0
	s_waitcnt vmcnt(3) lgkmcnt(1)
	v_mfma_f32_32x32x16_f16 v[18:33], v[34:37], v[136:139], v[2:17]
	s_waitcnt lgkmcnt(0)
	v_mfma_f32_32x32x16_f16 v[2:17], v[38:41], v[136:139], v[2:17]
	ds_read_b128 v[34:37], v198 offset:2048
	ds_read_b128 v[38:41], v198 offset:2560
	s_waitcnt vmcnt(2) lgkmcnt(1)
	v_mfma_f32_32x32x16_f16 v[18:33], v[34:37], v[128:131], v[18:33]
	s_waitcnt lgkmcnt(0)
	v_mfma_f32_32x32x16_f16 v[2:17], v[38:41], v[128:131], v[2:17]
	ds_read_b128 v[34:37], v198 offset:4096
	ds_read_b128 v[38:41], v198 offset:4608
	s_waitcnt vmcnt(1) lgkmcnt(1)
	v_mfma_f32_32x32x16_f16 v[18:33], v[34:37], v[120:123], v[18:33]
	s_waitcnt lgkmcnt(0)
	v_mfma_f32_32x32x16_f16 v[2:17], v[38:41], v[120:123], v[2:17]
	ds_read_b128 v[34:37], v198 offset:6144
	ds_read_b128 v[38:41], v198 offset:6656
	s_waitcnt vmcnt(0) lgkmcnt(1)
	v_mfma_f32_32x32x16_f16 v[18:33], v[34:37], v[116:119], v[18:33]
	s_waitcnt lgkmcnt(0)
	v_mfma_f32_32x32x16_f16 v[2:17], v[38:41], v[116:119], v[2:17]
	s_nop 9
	v_max_f32_e32 v1, v19, v19
	v_max_f32_e32 v34, v18, v18
	v_max_f32_e32 v1, v34, v1
	v_max3_f32 v35, v20, v21, v3
	v_max3_f32 v1, v1, v2, v4
	v_max3_f32 v34, v35, v24, v25
	v_max3_f32 v1, v1, v5, v22
	v_max3_f32 v34, v34, v8, v9
	v_max3_f32 v1, v1, v23, v6
	v_max3_f32 v34, v34, v28, v29
	v_max3_f32 v1, v1, v7, v26
	v_max3_f32 v34, v34, v12, v13
	v_max3_f32 v1, v1, v27, v10
	v_max3_f32 v34, v34, v32, v33
	v_max3_f32 v1, v1, v11, v30
	v_max3_f32 v34, v34, v16, v17
	v_max3_f32 v1, v1, v31, v14
	v_max3_f32 v1, v1, v15, v34
	v_mov_b32_e32 v34, v1
	s_nop 1
	v_permlane32_swap_b32_e32 v1, v34
	v_max_f32_e32 v34, v34, v34
	v_max_f32_e32 v1, v1, v1
	v_max_f32_e32 v197, v1, v34
	v_lshlrev_b32_e32 v1, 1, v0
	v_sub_f32_e32 v62, v32, v197
	v_and_b32_e32 v1, 32, v1
	v_and_b32_e32 v32, 24, v193
	v_lshlrev_b32_e32 v0, 4, v0
	v_add3_u32 v1, 0, v1, v32
	v_and_b32_e32 v0, 0xc0, v0
	v_lshlrev_b32_e32 v32, 8, v192
	v_add3_u32 v194, v1, v32, v0
	v_xor_b32_e32 v32, 0x80000000, v197
	v_sub_f32_e32 v63, v33, v197
	v_mov_b32_e32 v33, v32
	v_mov_b32_e32 v34, v32
	v_mov_b32_e32 v35, v32
	v_mov_b32_e32 v36, v32
	v_mov_b32_e32 v37, v32
	v_mov_b32_e32 v38, v32
	v_mov_b32_e32 v39, v32
	v_mov_b32_e32 v40, v32
	v_mov_b32_e32 v41, v32
	v_mov_b32_e32 v42, v32
	v_mov_b32_e32 v43, v32
	v_mov_b32_e32 v44, v32
	v_mov_b32_e32 v45, v32
	v_mov_b32_e32 v46, v32
	v_mov_b32_e32 v47, v32
	s_waitcnt vmcnt(0) lgkmcnt(0)
	s_barrier
	v_lshl_add_u64 v[0:1], v[48:49], 0, s[16:17]
	s_mov_b32 s12, m0
	s_mov_b32 m0, s1
	s_nop 0
	global_load_lds_dwordx4 v[0:1], off
	s_mov_b32 m0, s12
	s_mov_b64 s[12:13], 0x806000
	v_lshl_add_u64 v[0:1], v[48:49], 0, s[12:13]
	s_mov_b32 s1, m0
	s_mov_b32 m0, s30
	s_nop 0
	global_load_lds_dwordx4 v[0:1], off
	s_mov_b32 m0, s1
	ds_read_b128 v[172:175], v198 offset:8192
	ds_read_b128 v[168:171], v198 offset:8704
	ds_read_b128 v[164:167], v198 offset:10240
	ds_read_b128 v[160:163], v198 offset:10752
	ds_read_b128 v[156:159], v198 offset:12288
	ds_read_b128 v[152:155], v198 offset:12800
	ds_read_b128 v[148:151], v198 offset:14336
	ds_read_b128 v[144:147], v198 offset:14848
	v_sub_f32_e32 v18, v18, v197
	v_sub_f32_e32 v19, v19, v197
	v_sub_f32_e32 v20, v20, v197
	v_sub_f32_e32 v21, v21, v197
	v_sub_f32_e32 v22, v22, v197
	v_sub_f32_e32 v23, v23, v197
	v_sub_f32_e32 v24, v24, v197
	v_sub_f32_e32 v25, v25, v197
	v_sub_f32_e32 v26, v26, v197
	v_sub_f32_e32 v27, v27, v197
	v_sub_f32_e32 v28, v28, v197
	v_sub_f32_e32 v29, v29, v197
	v_sub_f32_e32 v30, v30, v197
	v_sub_f32_e32 v31, v31, v197
	v_sub_f32_e32 v2, v2, v197
	v_sub_f32_e32 v3, v3, v197
	v_sub_f32_e32 v4, v4, v197
	v_sub_f32_e32 v5, v5, v197
	v_sub_f32_e32 v6, v6, v197
	v_sub_f32_e32 v7, v7, v197
	v_sub_f32_e32 v8, v8, v197
	v_sub_f32_e32 v9, v9, v197
	v_sub_f32_e32 v10, v10, v197
	v_sub_f32_e32 v11, v11, v197
	v_sub_f32_e32 v12, v12, v197
	v_sub_f32_e32 v13, v13, v197
	v_sub_f32_e32 v14, v14, v197
	v_sub_f32_e32 v15, v15, v197
	v_sub_f32_e32 v16, v16, v197
	v_sub_f32_e32 v17, v17, v197
	v_exp_f32_e32 v64, v18
	v_exp_f32_e32 v65, v19
	v_exp_f32_e32 v48, v2
	v_exp_f32_e32 v49, v3
	v_exp_f32_e32 v66, v20
	v_exp_f32_e32 v50, v4
	v_mov_b32_e32 v67, v21
	v_mov_b32_e32 v51, v5
	v_exp_f32_e32 v68, v22
	v_exp_f32_e32 v52, v6
	v_exp_f32_e32 v69, v23
	v_exp_f32_e32 v53, v7
	v_exp_f32_e32 v70, v24
	v_exp_f32_e32 v54, v8
	v_mov_b32_e32 v71, v25
	v_mov_b32_e32 v55, v9
	v_exp_f32_e32 v72, v26
	v_exp_f32_e32 v56, v10
	v_exp_f32_e32 v73, v27
	v_exp_f32_e32 v57, v11
	v_exp_f32_e32 v74, v28
	v_exp_f32_e32 v58, v12
	v_mov_b32_e32 v75, v29
	v_mov_b32_e32 v59, v13
	v_exp_f32_e32 v76, v30
	v_exp_f32_e32 v60, v14
	v_exp_f32_e32 v77, v31
	v_exp_f32_e32 v61, v15
	v_exp_f32_e32 v78, v62
	v_exp_f32_e32 v62, v16
	v_mov_b32_e32 v79, v63
	v_mov_b32_e32 v63, v17
	s_waitcnt vmcnt(2) lgkmcnt(0)
	s_barrier
	v_or_b32_e32 v0, s2, v184
	v_mov_b32_e32 v1, s3
	v_lshl_add_u64 v[186:187], s[4:5], 0, v[0:1]
	s_mov_b32 s2, 0xff800000
	s_mov_b32 s4, 0xff806000
	v_cmp_gt_u32_e64 s[0:1], 32, v190
	s_mov_b32 s3, -1
	s_mov_b32 s5, -1
	s_mov_b64 s[12:13], 0x8000
	v_mov_b32_e32 v0, 0
	v_mov_b32_e32 v1, v185
	v_mov_b32_e32 v2, v185
	v_mov_b32_e32 v3, v185
	v_mov_b32_e32 v4, v185
	v_mov_b32_e32 v5, v185
	v_mov_b32_e32 v6, v185
	v_mov_b32_e32 v7, v185
	v_mov_b32_e32 v8, v185
	v_mov_b32_e32 v9, v185
	v_mov_b32_e32 v10, v185
	v_mov_b32_e32 v11, v185
	v_mov_b32_e32 v12, v185
	v_mov_b32_e32 v13, v185
	v_mov_b32_e32 v14, v185
	v_mov_b32_e32 v15, v185
	v_mov_b32_e32 v16, 0
	v_mov_b32_e32 v17, v185
	v_mov_b32_e32 v18, v185
	v_mov_b32_e32 v19, v185
	v_mov_b32_e32 v20, v185
	v_mov_b32_e32 v21, v185
	v_mov_b32_e32 v22, v185
	v_mov_b32_e32 v23, v185
	v_mov_b32_e32 v24, v185
	v_mov_b32_e32 v25, v185
	v_mov_b32_e32 v26, v185
	v_mov_b32_e32 v27, v185
	v_mov_b32_e32 v28, v185
	v_mov_b32_e32 v29, v185
	v_mov_b32_e32 v30, v185
	v_mov_b32_e32 v31, v185
	v_lshl_add_u64 v[188:189], v[186:187], 0, s[16:17]
	.p2align	6

amdhsa.kernels:
  - .agpr_count:     0
    .args:
      - .actual_access:  read_only
        .address_space:  global
        .offset:         0
        .size:           8
        .value_kind:     global_buffer
      - .actual_access:  read_only
        .address_space:  global
        .offset:         8
        .size:           8
        .value_kind:     global_buffer
      - .actual_access:  read_only
        .address_space:  global
        .offset:         16
        .size:           8
        .value_kind:     global_buffer
      - .actual_access:  read_only
        .address_space:  global
        .offset:         24
        .size:           8
        .value_kind:     global_buffer
      - .actual_access:  read_only
        .address_space:  global
        .offset:         32
        .size:           8
        .value_kind:     global_buffer
      - .actual_access:  write_only
        .address_space:  global
        .offset:         40
        .size:           8
        .value_kind:     global_buffer
      - .actual_access:  read_only
        .address_space:  global
        .offset:         48
        .size:           8
        .value_kind:     global_buffer
      - .actual_access:  read_only
        .address_space:  global
        .offset:         56
        .size:           8
        .value_kind:     global_buffer
      - .actual_access:  read_only
        .address_space:  global
        .offset:         64
        .size:           8
        .value_kind:     global_buffer
      - .actual_access:  write_only
        .address_space:  global
        .offset:         72
        .size:           8
        .value_kind:     global_buffer
    .group_segment_fixed_size: 0
    .kernarg_segment_align: 8
    .kernarg_segment_size: 80
    .language:       OpenCL C
    .language_version:
      - 2
      - 0
    .max_flat_workgroup_size: 256
    .name:           _Z7cvt_allPKfS0_S0_S0_S0_PDF16_S0_S0_S0_Pf
    .private_segment_fixed_size: 0
    .sgpr_count:     16
    .sgpr_spill_count: 0
    .symbol:         _Z7cvt_allPKfS0_S0_S0_S0_PDF16_S0_S0_S0_Pf.kd
    .uniform_work_group_size: 1
    .uses_dynamic_stack: false
    .vgpr_count:     26
    .vgpr_spill_count: 0
    .wavefront_size: 64
  - .agpr_count:     0
    .args:
      - .address_space:  global
        .offset:         0
        .size:           8
        .value_kind:     global_buffer
      - .address_space:  global
        .offset:         8
        .size:           8
        .value_kind:     global_buffer
      - .actual_access:  read_only
        .address_space:  global
        .offset:         16
        .size:           8
        .value_kind:     global_buffer
      - .actual_access:  write_only
        .address_space:  global
        .offset:         24
        .size:           8
        .value_kind:     global_buffer
      - .offset:         32
        .size:           4
        .value_kind:     hidden_block_count_x
      - .offset:         36
        .size:           4
        .value_kind:     hidden_block_count_y
      - .offset:         40
        .size:           4
        .value_kind:     hidden_block_count_z
      - .offset:         44
        .size:           2
        .value_kind:     hidden_group_size_x
      - .offset:         46
        .size:           2
        .value_kind:     hidden_group_size_y
      - .offset:         48
        .size:           2
        .value_kind:     hidden_group_size_z
      - .offset:         50
        .size:           2
        .value_kind:     hidden_remainder_x
      - .offset:         52
        .size:           2
        .value_kind:     hidden_remainder_y
      - .offset:         54
        .size:           2
        .value_kind:     hidden_remainder_z
      - .offset:         72
        .size:           8
        .value_kind:     hidden_global_offset_x
      - .offset:         80
        .size:           8
        .value_kind:     hidden_global_offset_y
      - .offset:         88
        .size:           8
        .value_kind:     hidden_global_offset_z
      - .offset:         96
        .size:           2
        .value_kind:     hidden_grid_dims
      - .offset:         152
        .size:           4
        .value_kind:     hidden_dynamic_lds_size
    .group_segment_fixed_size: 0
    .kernarg_segment_align: 8
    .kernarg_segment_size: 288
    .language:       OpenCL C
    .language_version:
      - 2
      - 0
    .max_flat_workgroup_size: 512
    .name:           _ZN6g128w88gemm_outEPKDF16_S1_PKfPf
    .private_segment_fixed_size: 0
    .sgpr_count:     29
    .sgpr_spill_count: 0
    .symbol:         _ZN6g128w88gemm_outEPKDF16_S1_PKfPf.kd
    .uniform_work_group_size: 1
    .uses_dynamic_stack: false
    .vgpr_count:     116
    .vgpr_spill_count: 0
    .wavefront_size: 64
  - .agpr_count:     0
    .args:
      - .address_space:  global
        .offset:         0
        .size:           8
        .value_kind:     global_buffer
      - .address_space:  global
        .offset:         8
        .size:           8
        .value_kind:     global_buffer
      - .actual_access:  read_only
        .address_space:  global
        .offset:         16
        .size:           8
        .value_kind:     global_buffer
      - .actual_access:  write_only
        .address_space:  global
        .offset:         24
        .size:           8
        .value_kind:     global_buffer
    .group_segment_fixed_size: 0
    .kernarg_segment_align: 8
    .kernarg_segment_size: 32
    .language:       OpenCL C
    .language_version:
      - 2
      - 0
    .max_flat_workgroup_size: 512
    .name:           _ZN4g2568gemm_qkvEPKDF16_S1_PKfPDF16_
    .private_segment_fixed_size: 0
    .sgpr_count:     52
    .sgpr_spill_count: 0
    .symbol:         _ZN4g2568gemm_qkvEPKDF16_S1_PKfPDF16_.kd
    .uniform_work_group_size: 1
    .uses_dynamic_stack: false
    .vgpr_count:     206
    .vgpr_spill_count: 0
    .wavefront_size: 64
  - .agpr_count:     0
    .args:
      - .address_space:  global
        .offset:         0
        .size:           8
        .value_kind:     global_buffer
      - .actual_access:  write_only
        .address_space:  global
        .offset:         8
        .size:           8
        .value_kind:     global_buffer
    .group_segment_fixed_size: 0
    .kernarg_segment_align: 8
    .kernarg_segment_size: 16
    .language:       OpenCL C
    .language_version:
      - 2
      - 0
    .max_flat_workgroup_size: 512
    .name:           _ZN3att8attn_fwdEPKDF16_PDF16_
    .private_segment_fixed_size: 0
    .sgpr_count:     42
    .sgpr_spill_count: 0
    .symbol:         _ZN3att8attn_fwdEPKDF16_PDF16_.kd
    .uniform_work_group_size: 1
    .uses_dynamic_stack: false
    .vgpr_count:     204
    .vgpr_spill_count: 0
    .wavefront_size: 64
